# prep: LN1 output (A1) dwordx2 stores sc1 on top of v19
# speedup vs baseline: 1.0063x; 1.0063x over previous
_Z10k_prep_ln18PrepArgsPKfS1_S1_Pt:
	s_load_dword s3, s[0:1], 0x100
	s_mov_b64 s[4:5], -1
	s_waitcnt lgkmcnt(0)
	s_addk_i32 s3, 0xff00
	s_cmp_lt_i32 s2, s3
	s_cbranch_scc1 .LBB0_2
	s_load_dwordx8 s[4:11], s[0:1], 0xe0
	v_lshlrev_b32_e32 v2, 2, v0
	v_lshrrev_b32_e32 v1, 3, v0
	v_and_b32_e32 v50, 0xfc, v2
	s_sub_i32 s3, s2, s3
	v_and_b32_e32 v1, 24, v1
	v_lshlrev_b32_e32 v46, 2, v50
	v_mov_b32_e32 v47, 0
	v_lshl_or_b32 v1, s3, 5, v1
	s_waitcnt lgkmcnt(0)
	v_lshl_add_u64 v[48:49], s[4:5], 0, v[46:47]
	s_movk_i32 s3, 0xc00
	v_mad_u64_u32 v[2:3], s[4:5], v1, s3, v[48:49]
	global_load_dwordx4 v[16:19], v[2:3], off
	global_load_dwordx4 v[42:45], v[2:3], off offset:1024
	global_load_dwordx4 v[38:41], v[2:3], off offset:2048
	v_or_b32_e32 v64, 1, v1
	v_mad_u64_u32 v[2:3], s[4:5], v64, s3, v[48:49]
	global_load_dwordx4 v[34:37], v[2:3], off
	global_load_dwordx4 v[30:33], v[2:3], off offset:1024
	global_load_dwordx4 v[26:29], v[2:3], off offset:2048
	v_mbcnt_lo_u32_b32 v2, -1, 0
	v_mbcnt_hi_u32_b32 v51, -1, v2
	v_and_b32_e32 v3, 64, v51
	v_xor_b32_e32 v5, 32, v51
	v_add_u32_e32 v57, 64, v3
	v_cmp_lt_i32_e32 vcc, v5, v57
	v_mov_b32_e32 v2, v47
	v_mov_b32_e32 v4, v47
	v_cndmask_b32_e32 v3, v51, v5, vcc
	v_lshlrev_b32_e32 v58, 2, v3
	v_xor_b32_e32 v52, 16, v51
	v_cmp_lt_i32_e32 vcc, v52, v57
	v_xor_b32_e32 v53, 8, v51
	v_xor_b32_e32 v54, 4, v51
	v_xor_b32_e32 v55, 2, v51
	v_xor_b32_e32 v56, 1, v51
	s_mov_b32 s12, 0x3727c5ac
	s_mov_b32 s4, 0x3aaaaaab
	v_or_b32_e32 v72, 2, v1
	v_or_b32_e32 v73, 3, v1
	s_waitcnt vmcnt(5)
	v_mov_b32_e32 v6, v17
	v_mov_b32_e32 v7, v18
	v_mov_b32_e32 v8, v16
	v_mov_b32_e32 v9, v19
	s_waitcnt vmcnt(4)
	v_add_f32_e32 v10, v42, v43
	v_add_f32_e32 v12, v44, v45
	s_waitcnt vmcnt(3)
	v_mov_b32_e32 v11, v40
	v_mov_b32_e32 v13, v41
	s_waitcnt vmcnt(2)
	v_mov_b32_e32 v14, v35
	v_mov_b32_e32 v15, v36
	v_mov_b32_e32 v20, v34
	v_mov_b32_e32 v21, v37
	v_pk_add_f32 v[6:7], v[6:7], v[8:9]
	v_pk_add_f32 v[8:9], v[10:11], v[12:13]
	v_pk_add_f32 v[10:11], v[14:15], v[20:21]
	v_pk_add_f32 v[6:7], v[6:7], v[6:7] op_sel:[0,1] op_sel_hi:[1,0]
	v_mov_b32_e32 v3, v39
	v_pk_add_f32 v[10:11], v[10:11], v[10:11] op_sel:[0,1] op_sel_hi:[1,0]
	v_mov_b32_e32 v7, v38
	s_waitcnt vmcnt(1)
	v_add_f32_e32 v22, v30, v31
	v_add_f32_e32 v24, v32, v33
	s_waitcnt vmcnt(0)
	v_mov_b32_e32 v5, v27
	v_mov_b32_e32 v23, v28
	v_mov_b32_e32 v25, v29
	v_mov_b32_e32 v11, v26
	v_pk_add_f32 v[2:3], v[6:7], v[2:3]
	v_pk_add_f32 v[12:13], v[22:23], v[24:25]
	v_pk_add_f32 v[4:5], v[10:11], v[4:5]
	v_pk_add_f32 v[2:3], v[2:3], v[8:9]
	v_pk_add_f32 v[4:5], v[4:5], v[12:13]
	v_add_f32_e32 v2, v2, v3
	v_add_f32_e32 v3, v4, v5
	ds_bpermute_b32 v4, v58, v2
	ds_bpermute_b32 v5, v58, v3
	v_cndmask_b32_e32 v6, v51, v52, vcc
	v_lshlrev_b32_e32 v59, 2, v6
	v_cmp_lt_i32_e32 vcc, v53, v57
	s_waitcnt lgkmcnt(1)
	v_add_f32_e32 v2, v2, v4
	ds_bpermute_b32 v4, v59, v2
	s_waitcnt lgkmcnt(1)
	v_add_f32_e32 v3, v3, v5
	ds_bpermute_b32 v5, v59, v3
	v_cndmask_b32_e32 v6, v51, v53, vcc
	v_lshlrev_b32_e32 v60, 2, v6
	s_waitcnt lgkmcnt(1)
	v_add_f32_e32 v2, v2, v4
	ds_bpermute_b32 v4, v60, v2
	s_waitcnt lgkmcnt(1)
	v_add_f32_e32 v3, v3, v5
	ds_bpermute_b32 v5, v60, v3
	v_cmp_lt_i32_e32 vcc, v54, v57
	v_mov_b64_e32 v[52:53], s[12:13]
	s_waitcnt lgkmcnt(1)
	v_add_f32_e32 v2, v2, v4
	v_cndmask_b32_e32 v6, v51, v54, vcc
	v_lshlrev_b32_e32 v61, 2, v6
	ds_bpermute_b32 v4, v61, v2
	s_waitcnt lgkmcnt(1)
	v_add_f32_e32 v3, v3, v5
	ds_bpermute_b32 v5, v61, v3
	v_cmp_lt_i32_e32 vcc, v55, v57
	s_waitcnt lgkmcnt(1)
	v_add_f32_e32 v2, v2, v4
	v_cndmask_b32_e32 v6, v51, v55, vcc
	v_lshlrev_b32_e32 v62, 2, v6
	ds_bpermute_b32 v4, v62, v2
	s_waitcnt lgkmcnt(1)
	v_add_f32_e32 v3, v3, v5
	ds_bpermute_b32 v5, v62, v3
	v_cmp_lt_i32_e32 vcc, v56, v57
	s_waitcnt lgkmcnt(1)
	v_add_f32_e32 v2, v2, v4
	v_cndmask_b32_e32 v6, v51, v56, vcc
	v_lshlrev_b32_e32 v63, 2, v6
	ds_bpermute_b32 v4, v63, v2
	s_waitcnt lgkmcnt(1)
	v_add_f32_e32 v3, v3, v5
	ds_bpermute_b32 v5, v63, v3
	s_waitcnt lgkmcnt(1)
	v_add_f32_e32 v2, v2, v4
	v_fmamk_f32 v20, v2, 0xbaaaaaab, v16
	v_fmac_f32_e32 v18, 0xbaaaaaab, v2
	v_fmamk_f32 v66, v2, 0xbaaaaaab, v42
	v_fmac_f32_e32 v44, 0xbaaaaaab, v2
	v_fmamk_f32 v21, v2, 0xbaaaaaab, v17
	v_fmamk_f32 v19, v2, 0xbaaaaaab, v19
	v_fmamk_f32 v67, v2, 0xbaaaaaab, v43
	v_fmamk_f32 v45, v2, 0xbaaaaaab, v45
	v_fmamk_f32 v41, v2, 0xbaaaaaab, v41
	v_fmamk_f32 v40, v2, 0xbaaaaaab, v40
	v_fmamk_f32 v39, v2, 0xbaaaaaab, v39
	v_fmac_f32_e32 v38, 0xbaaaaaab, v2
	v_mul_f32_e32 v2, v20, v20
	v_mul_f32_e32 v4, v18, v18
	v_mul_f32_e32 v6, v66, v66
	v_mul_f32_e32 v8, v44, v44
	s_waitcnt lgkmcnt(0)
	v_add_f32_e32 v22, v3, v5
	v_pk_fma_f32 v[2:3], v[20:21], v[20:21], v[2:3] op_sel_hi:[1,1,0]
	v_pk_fma_f32 v[4:5], v[18:19], v[18:19], v[4:5] op_sel_hi:[1,1,0]
	v_pk_fma_f32 v[6:7], v[66:67], v[66:67], v[6:7] op_sel_hi:[1,1,0]
	v_pk_fma_f32 v[8:9], v[44:45], v[44:45], v[8:9] op_sel_hi:[1,1,0]
	v_mul_f32_e32 v2, v38, v38
	v_mul_f32_e32 v4, v39, v39
	v_mul_f32_e32 v6, v40, v40
	v_mul_f32_e32 v8, v41, v41
	v_pk_add_f32 v[2:3], v[2:3], v[4:5]
	v_pk_add_f32 v[4:5], v[6:7], v[8:9]
	v_fmamk_f32 v42, v22, 0xbaaaaaab, v34
	v_fmamk_f32 v43, v22, 0xbaaaaaab, v35
	v_pk_add_f32 v[10:11], v[2:3], v[4:5]
	v_fmac_f32_e32 v36, 0xbaaaaaab, v22
	v_mul_f32_e32 v2, v42, v42
	v_fmamk_f32 v37, v22, 0xbaaaaaab, v37
	v_pk_fma_f32 v[12:13], v[42:43], v[42:43], v[2:3] op_sel_hi:[1,1,0]
	v_mul_f32_e32 v2, v36, v36
	v_pk_fma_f32 v[14:15], v[36:37], v[36:37], v[2:3] op_sel_hi:[1,1,0]
	global_load_dwordx4 v[2:5], v46, s[6:7]
	global_load_dwordx4 v[6:9], v46, s[8:9]
	v_fmamk_f32 v56, v22, 0xbaaaaaab, v30
	v_fmamk_f32 v57, v22, 0xbaaaaaab, v31
	v_mul_f32_e32 v12, v56, v56
	v_fmamk_f32 v27, v22, 0xbaaaaaab, v27
	v_fmac_f32_e32 v26, 0xbaaaaaab, v22
	v_fmac_f32_e32 v32, 0xbaaaaaab, v22
	v_pk_fma_f32 v[16:17], v[56:57], v[56:57], v[12:13] op_sel_hi:[1,1,0]
	v_mul_f32_e32 v12, v26, v26
	v_mul_f32_e32 v14, v27, v27
	v_fmamk_f32 v33, v22, 0xbaaaaaab, v33
	v_pk_add_f32 v[12:13], v[12:13], v[14:15]
	v_mul_f32_e32 v14, v32, v32
	v_fmamk_f32 v55, v22, 0xbaaaaaab, v29
	v_fmamk_f32 v54, v22, 0xbaaaaaab, v28
	v_pk_fma_f32 v[14:15], v[32:33], v[32:33], v[14:15] op_sel_hi:[1,1,0]
	v_mul_f32_e32 v16, v54, v54
	v_mul_f32_e32 v14, v55, v55
	v_pk_add_f32 v[14:15], v[16:17], v[14:15]
	s_nop 0
	v_pk_add_f32 v[12:13], v[12:13], v[14:15]
	v_mov_b32_e32 v15, v10
	v_mov_b32_e32 v14, v12
	v_mov_b32_e32 v10, v13
	v_pk_add_f32 v[10:11], v[14:15], v[10:11]
	ds_bpermute_b32 v13, v58, v11
	ds_bpermute_b32 v12, v58, v10
	s_waitcnt lgkmcnt(0)
	v_pk_add_f32 v[10:11], v[10:11], v[12:13]
	ds_bpermute_b32 v13, v59, v11
	ds_bpermute_b32 v12, v59, v10
	s_waitcnt lgkmcnt(0)
	v_pk_add_f32 v[10:11], v[10:11], v[12:13]
	ds_bpermute_b32 v13, v60, v11
	ds_bpermute_b32 v12, v60, v10
	s_waitcnt lgkmcnt(0)
	v_pk_add_f32 v[10:11], v[10:11], v[12:13]
	ds_bpermute_b32 v13, v61, v11
	ds_bpermute_b32 v12, v61, v10
	s_waitcnt lgkmcnt(0)
	v_pk_add_f32 v[10:11], v[10:11], v[12:13]
	ds_bpermute_b32 v13, v62, v11
	ds_bpermute_b32 v12, v62, v10
	s_waitcnt lgkmcnt(0)
	v_pk_add_f32 v[10:11], v[10:11], v[12:13]
	ds_bpermute_b32 v13, v63, v11
	ds_bpermute_b32 v12, v63, v10
	s_waitcnt lgkmcnt(0)
	v_pk_add_f32 v[22:23], v[10:11], v[12:13]
	global_load_dwordx4 v[10:13], v46, s[6:7] offset:1024
	global_load_dwordx4 v[14:17], v46, s[8:9] offset:1024
	v_pk_fma_f32 v[28:29], v[22:23], s[4:5], v[52:53] op_sel_hi:[1,0,0]
	s_mov_b32 s5, 0x800000
	v_mul_f32_e32 v22, 0x4b800000, v29
	v_cmp_gt_f32_e32 vcc, s5, v29
	s_nop 1
	v_cndmask_b32_e32 v22, v29, v22, vcc
	v_rsq_f32_e32 v22, v22
	v_mul_f32_e32 v29, 0x4b800000, v28
	v_mul_f32_e32 v23, 0x45800000, v22
	v_cndmask_b32_e32 v30, v22, v23, vcc
	v_pk_mul_f32 v[20:21], v[20:21], v[30:31] op_sel_hi:[1,0]
	v_pk_mul_f32 v[18:19], v[18:19], v[30:31] op_sel_hi:[1,0]
	s_waitcnt vmcnt(2)
	v_pk_fma_f32 v[20:21], v[2:3], v[20:21], v[6:7]
	v_pk_fma_f32 v[18:19], v[4:5], v[18:19], v[8:9]
	v_cvt_pk_f16_f32 v34, v20, v21
	v_cvt_pk_f16_f32 v35, v18, v19
	global_load_dwordx4 v[18:21], v46, s[6:7] offset:2048
	global_load_dwordx4 v[22:25], v46, s[8:9] offset:2048
	v_lshlrev_b32_e32 v46, 1, v50
	s_movk_i32 s6, 0x600
	v_lshl_add_u64 v[50:51], s[10:11], 0, v[46:47]
	v_mad_u64_u32 v[68:69], s[8:9], v1, s6, v[50:51]
	global_store_dwordx2 v[68:69], v[34:35], off sc1
	v_pk_mul_f32 v[34:35], v[44:45], v[30:31] op_sel_hi:[1,0]
	v_pk_mul_f32 v[44:45], v[66:67], v[30:31] op_sel_hi:[1,0]
	v_cmp_gt_f32_e32 vcc, s5, v28
	v_mad_u64_u32 v[64:65], s[8:9], v64, s6, v[50:51]
	s_waitcnt vmcnt(3)
	v_pk_fma_f32 v[34:35], v[12:13], v[34:35], v[16:17]
	v_pk_fma_f32 v[44:45], v[10:11], v[44:45], v[14:15]
	s_nop 0
	v_cvt_pk_f16_f32 v44, v44, v45
	v_cvt_pk_f16_f32 v45, v34, v35
	global_store_dwordx2 v[68:69], v[44:45], off offset:512 sc1
	v_mad_u64_u32 v[44:45], s[8:9], v72, s3, v[48:49]
	v_pk_mul_f32 v[34:35], v[38:39], v[30:31] op_sel_hi:[1,0]
	v_pk_mul_f32 v[38:39], v[40:41], v[30:31] op_sel_hi:[1,0]
	v_cndmask_b32_e32 v40, v28, v29, vcc
	global_load_dwordx4 v[28:31], v[44:45], off
	v_rsq_f32_e32 v46, v40
	s_waitcnt vmcnt(3)
	v_pk_fma_f32 v[38:39], v[20:21], v[38:39], v[24:25]
	v_pk_fma_f32 v[34:35], v[18:19], v[34:35], v[22:23]
	s_nop 0
	v_cvt_pk_f16_f32 v34, v34, v35
	v_cvt_pk_f16_f32 v35, v38, v39
	global_store_dwordx2 v[68:69], v[34:35], off offset:1024 sc1
	v_mul_f32_e32 v34, 0x45800000, v46
	global_load_dwordx4 v[38:41], v[44:45], off offset:2048
	v_cndmask_b32_e32 v46, v46, v34, vcc
	v_pk_mul_f32 v[66:67], v[36:37], v[46:47] op_sel_hi:[1,0]
	global_load_dwordx4 v[34:37], v[44:45], off offset:1024
	v_pk_mul_f32 v[42:43], v[42:43], v[46:47] op_sel_hi:[1,0]
	v_pk_fma_f32 v[44:45], v[4:5], v[66:67], v[8:9]
	v_pk_fma_f32 v[42:43], v[2:3], v[42:43], v[6:7]
	v_pk_mul_f32 v[32:33], v[32:33], v[46:47] op_sel_hi:[1,0]
	v_cvt_pk_f16_f32 v42, v42, v43
	v_cvt_pk_f16_f32 v43, v44, v45
	global_store_dwordx2 v[64:65], v[42:43], off sc1
	v_pk_mul_f32 v[42:43], v[56:57], v[46:47] op_sel_hi:[1,0]
	v_pk_fma_f32 v[32:33], v[12:13], v[32:33], v[16:17]
	v_pk_fma_f32 v[42:43], v[10:11], v[42:43], v[14:15]
	v_mad_u64_u32 v[66:67], s[8:9], v73, s3, v[48:49]
	v_cvt_pk_f16_f32 v42, v42, v43
	v_cvt_pk_f16_f32 v43, v32, v33
	global_store_dwordx2 v[64:65], v[42:43], off offset:512 sc1
	v_mov_b32_e32 v56, v47
	v_pk_mul_f32 v[26:27], v[26:27], v[46:47] op_sel_hi:[1,0]
	s_waitcnt vmcnt(5)
	v_mov_b32_e32 v32, v29
	v_mov_b32_e32 v33, v30
	v_mov_b32_e32 v42, v28
	v_mov_b32_e32 v43, v31
	v_pk_add_f32 v[32:33], v[32:33], v[42:43]
	global_load_dwordx4 v[42:45], v[66:67], off
	v_pk_add_f32 v[32:33], v[32:33], v[32:33] op_sel:[0,1] op_sel_hi:[1,0]
	v_pk_fma_f32 v[26:27], v[18:19], v[26:27], v[22:23]
	s_waitcnt vmcnt(4)
	v_mov_b32_e32 v33, v38
	v_mov_b32_e32 v57, v39
	v_pk_add_f32 v[32:33], v[32:33], v[56:57]
	s_waitcnt vmcnt(3)
	v_add_f32_e32 v56, v34, v35
	v_mov_b32_e32 v57, v40
	v_add_f32_e32 v68, v36, v37
	v_mov_b32_e32 v69, v41
	v_pk_add_f32 v[56:57], v[56:57], v[68:69]
	v_cvt_pk_f16_f32 v26, v26, v27
	v_pk_add_f32 v[32:33], v[32:33], v[56:57]
	s_nop 0
	v_add_f32_e32 v32, v32, v33
	ds_bpermute_b32 v33, v58, v32
	s_waitcnt lgkmcnt(0)
	v_add_f32_e32 v32, v32, v33
	ds_bpermute_b32 v33, v59, v32
	s_waitcnt lgkmcnt(0)
	v_add_f32_e32 v32, v32, v33
	ds_bpermute_b32 v33, v60, v32
	s_waitcnt lgkmcnt(0)
	v_add_f32_e32 v32, v32, v33
	ds_bpermute_b32 v33, v61, v32
	s_waitcnt lgkmcnt(0)
	v_add_f32_e32 v56, v32, v33
	ds_bpermute_b32 v57, v62, v56
	v_pk_mul_f32 v[32:33], v[54:55], v[46:47] op_sel_hi:[1,0]
	s_waitcnt lgkmcnt(0)
	v_add_f32_e32 v46, v56, v57
	ds_bpermute_b32 v54, v63, v46
	v_pk_fma_f32 v[32:33], v[20:21], v[32:33], v[24:25]
	s_waitcnt lgkmcnt(0)
	v_add_f32_e32 v46, v46, v54
	v_cvt_pk_f16_f32 v27, v32, v33
	v_fmamk_f32 v32, v46, 0xbaaaaaab, v28
	global_store_dwordx2 v[64:65], v[26:27], off offset:1024 sc1
	v_fmamk_f32 v33, v46, 0xbaaaaaab, v29
	v_mul_f32_e32 v26, v32, v32
	v_fmac_f32_e32 v30, 0xbaaaaaab, v46
	v_pk_fma_f32 v[26:27], v[32:33], v[32:33], v[26:27] op_sel_hi:[1,1,0]
	v_fmamk_f32 v31, v46, 0xbaaaaaab, v31
	v_mul_f32_e32 v26, v30, v30
	v_pk_fma_f32 v[28:29], v[30:31], v[30:31], v[26:27] op_sel_hi:[1,1,0]
	v_fmamk_f32 v39, v46, 0xbaaaaaab, v39
	v_fmac_f32_e32 v38, 0xbaaaaaab, v46
	v_mul_f32_e32 v26, v38, v38
	v_mul_f32_e32 v28, v39, v39
	v_fmamk_f32 v34, v46, 0xbaaaaaab, v34
	v_pk_add_f32 v[26:27], v[26:27], v[28:29]
	v_fmamk_f32 v35, v46, 0xbaaaaaab, v35
	v_mul_f32_e32 v28, v34, v34
	v_fmac_f32_e32 v36, 0xbaaaaaab, v46
	v_pk_fma_f32 v[28:29], v[34:35], v[34:35], v[28:29] op_sel_hi:[1,1,0]
	v_fmamk_f32 v37, v46, 0xbaaaaaab, v37
	v_mul_f32_e32 v28, v36, v36
	v_fmamk_f32 v41, v46, 0xbaaaaaab, v41
	v_fmamk_f32 v40, v46, 0xbaaaaaab, v40
	v_pk_fma_f32 v[54:55], v[36:37], v[36:37], v[28:29] op_sel_hi:[1,1,0]
	v_mul_f32_e32 v28, v40, v40
	v_mul_f32_e32 v54, v41, v41
	v_pk_add_f32 v[28:29], v[28:29], v[54:55]
	s_nop 0
	v_pk_add_f32 v[64:65], v[26:27], v[28:29]
	s_waitcnt vmcnt(1)
	v_mov_b32_e32 v26, v43
	v_mov_b32_e32 v27, v44
	v_mov_b32_e32 v28, v42
	v_mov_b32_e32 v29, v45
	v_pk_add_f32 v[26:27], v[26:27], v[28:29]
	s_nop 0
	v_pk_add_f32 v[68:69], v[26:27], v[26:27] op_sel:[0,1] op_sel_hi:[1,0]
	global_load_dwordx4 v[26:29], v[66:67], off offset:2048
	global_load_dwordx4 v[54:57], v[66:67], off offset:1024
	v_mov_b32_e32 v66, v47
	s_waitcnt vmcnt(1)
	v_mov_b32_e32 v69, v26
	v_mov_b32_e32 v67, v27
	v_pk_add_f32 v[66:67], v[68:69], v[66:67]
	s_waitcnt vmcnt(0)
	v_add_f32_e32 v68, v54, v55
	v_mov_b32_e32 v69, v28
	v_add_f32_e32 v70, v56, v57
	v_mov_b32_e32 v71, v29
	v_pk_add_f32 v[68:69], v[68:69], v[70:71]
	s_nop 0
	v_pk_add_f32 v[66:67], v[66:67], v[68:69]
	s_nop 0
	v_add_f32_e32 v46, v66, v67
	ds_bpermute_b32 v66, v58, v46
	s_waitcnt lgkmcnt(0)
	v_add_f32_e32 v46, v46, v66
	ds_bpermute_b32 v66, v59, v46
	s_waitcnt lgkmcnt(0)
	v_add_f32_e32 v46, v46, v66
	ds_bpermute_b32 v66, v60, v46
	s_waitcnt lgkmcnt(0)
	v_add_f32_e32 v46, v46, v66
	ds_bpermute_b32 v66, v61, v46
	s_waitcnt lgkmcnt(0)
	v_add_f32_e32 v46, v46, v66
	ds_bpermute_b32 v66, v62, v46
	s_waitcnt lgkmcnt(0)
	v_add_f32_e32 v46, v46, v66
	ds_bpermute_b32 v66, v63, v46
	s_waitcnt lgkmcnt(0)
	v_add_f32_e32 v70, v46, v66
	v_fmamk_f32 v42, v70, 0xbaaaaaab, v42
	v_fmamk_f32 v43, v70, 0xbaaaaaab, v43
	v_fmac_f32_e32 v44, 0xbaaaaaab, v70
	v_mul_f32_e32 v46, v42, v42
	v_fmamk_f32 v45, v70, 0xbaaaaaab, v45
	v_pk_fma_f32 v[66:67], v[42:43], v[42:43], v[46:47] op_sel_hi:[1,1,0]
	v_mul_f32_e32 v46, v44, v44
	v_pk_fma_f32 v[68:69], v[44:45], v[44:45], v[46:47] op_sel_hi:[1,1,0]
	v_fmamk_f32 v27, v70, 0xbaaaaaab, v27
	v_fmac_f32_e32 v26, 0xbaaaaaab, v70
	v_fmamk_f32 v54, v70, 0xbaaaaaab, v54
	v_mul_f32_e32 v66, v26, v26
	v_mul_f32_e32 v68, v27, v27
	v_fmamk_f32 v55, v70, 0xbaaaaaab, v55
	v_fmac_f32_e32 v56, 0xbaaaaaab, v70
	v_mul_f32_e32 v46, v54, v54
	v_pk_add_f32 v[66:67], v[66:67], v[68:69]
	v_fmamk_f32 v57, v70, 0xbaaaaaab, v57
	v_pk_fma_f32 v[68:69], v[54:55], v[54:55], v[46:47] op_sel_hi:[1,1,0]
	v_mul_f32_e32 v46, v56, v56
	v_fmamk_f32 v29, v70, 0xbaaaaaab, v29
	v_fmamk_f32 v28, v70, 0xbaaaaaab, v28
	v_pk_fma_f32 v[70:71], v[56:57], v[56:57], v[46:47] op_sel_hi:[1,1,0]
	v_mul_f32_e32 v68, v28, v28
	v_mul_f32_e32 v70, v29, v29
	v_pk_add_f32 v[68:69], v[68:69], v[70:71]
	s_nop 0
	v_pk_add_f32 v[66:67], v[66:67], v[68:69]
	v_mov_b32_e32 v69, v64
	v_mov_b32_e32 v68, v66
	v_mov_b32_e32 v64, v67
	v_pk_add_f32 v[64:65], v[68:69], v[64:65]
	ds_bpermute_b32 v67, v58, v65
	ds_bpermute_b32 v66, v58, v64
	s_waitcnt lgkmcnt(0)
	v_pk_add_f32 v[64:65], v[64:65], v[66:67]
	ds_bpermute_b32 v67, v59, v65
	ds_bpermute_b32 v66, v59, v64
	s_waitcnt lgkmcnt(0)
	v_pk_add_f32 v[64:65], v[64:65], v[66:67]
	ds_bpermute_b32 v67, v60, v65
	ds_bpermute_b32 v66, v60, v64
	s_waitcnt lgkmcnt(0)
	v_pk_add_f32 v[64:65], v[64:65], v[66:67]
	ds_bpermute_b32 v67, v61, v65
	ds_bpermute_b32 v66, v61, v64
	s_waitcnt lgkmcnt(0)
	v_pk_add_f32 v[64:65], v[64:65], v[66:67]
	ds_bpermute_b32 v67, v62, v65
	ds_bpermute_b32 v66, v62, v64
	s_waitcnt lgkmcnt(0)
	v_pk_add_f32 v[64:65], v[64:65], v[66:67]
	ds_bpermute_b32 v67, v63, v65
	ds_bpermute_b32 v66, v63, v64
	s_waitcnt lgkmcnt(0)
	v_pk_add_f32 v[64:65], v[64:65], v[66:67]
	s_nop 0
	v_pk_fma_f32 v[64:65], v[64:65], s[4:5], v[52:53] op_sel_hi:[1,0,0]
	v_mov_b32_e32 v66, v47
	v_mul_f32_e32 v46, 0x4b800000, v65
	v_cmp_gt_f32_e32 vcc, s5, v65
	s_nop 1
	v_cndmask_b32_e32 v46, v65, v46, vcc
	v_rsq_f32_e32 v46, v46
	s_nop 0
	v_mul_f32_e32 v65, 0x45800000, v46
	v_cndmask_b32_e32 v46, v46, v65, vcc
	v_pk_mul_f32 v[30:31], v[30:31], v[46:47] op_sel_hi:[1,0]
	v_pk_mul_f32 v[32:33], v[32:33], v[46:47] op_sel_hi:[1,0]
	v_pk_fma_f32 v[30:31], v[4:5], v[30:31], v[8:9]
	v_pk_fma_f32 v[32:33], v[2:3], v[32:33], v[6:7]
	v_pk_mul_f32 v[34:35], v[34:35], v[46:47] op_sel_hi:[1,0]
	v_cvt_pk_f16_f32 v32, v32, v33
	v_cvt_pk_f16_f32 v33, v30, v31
	v_mad_u64_u32 v[30:31], s[8:9], v72, s6, v[50:51]
	global_store_dwordx2 v[30:31], v[32:33], off sc1
	v_pk_mul_f32 v[32:33], v[36:37], v[46:47] op_sel_hi:[1,0]
	v_pk_fma_f32 v[34:35], v[10:11], v[34:35], v[14:15]
	v_pk_fma_f32 v[32:33], v[12:13], v[32:33], v[16:17]
	v_cvt_pk_f16_f32 v34, v34, v35
	v_cvt_pk_f16_f32 v35, v32, v33
	v_or_b32_e32 v72, 4, v1
	global_store_dwordx2 v[30:31], v[34:35], off offset:512 sc1
	v_pk_mul_f32 v[32:33], v[38:39], v[46:47] op_sel_hi:[1,0]
	v_pk_mul_f32 v[38:39], v[40:41], v[46:47] op_sel_hi:[1,0]
	v_mul_f32_e32 v34, 0x4b800000, v64
	v_cmp_gt_f32_e32 vcc, s5, v64
	v_mad_u64_u32 v[40:41], s[8:9], v72, s3, v[48:49]
	s_nop 0
	v_cndmask_b32_e32 v46, v64, v34, vcc
	global_load_dwordx4 v[34:37], v[40:41], off
	v_rsq_f32_e32 v46, v46
	v_pk_fma_f32 v[38:39], v[20:21], v[38:39], v[24:25]
	v_pk_fma_f32 v[32:33], v[18:19], v[32:33], v[22:23]
	v_mad_u64_u32 v[64:65], s[8:9], v73, s6, v[50:51]
	v_cvt_pk_f16_f32 v32, v32, v33
	v_cvt_pk_f16_f32 v33, v38, v39
	global_store_dwordx2 v[30:31], v[32:33], off offset:1024 sc1
	global_load_dwordx4 v[30:33], v[40:41], off offset:2048
	v_mul_f32_e32 v38, 0x45800000, v46
	v_cndmask_b32_e32 v46, v46, v38, vcc
	global_load_dwordx4 v[38:41], v[40:41], off offset:1024
	v_pk_mul_f32 v[44:45], v[44:45], v[46:47] op_sel_hi:[1,0]
	v_pk_mul_f32 v[42:43], v[42:43], v[46:47] op_sel_hi:[1,0]
	v_pk_fma_f32 v[44:45], v[4:5], v[44:45], v[8:9]
	v_pk_fma_f32 v[42:43], v[2:3], v[42:43], v[6:7]
	v_or_b32_e32 v73, 5, v1
	v_cvt_pk_f16_f32 v42, v42, v43
	v_cvt_pk_f16_f32 v43, v44, v45
	global_store_dwordx2 v[64:65], v[42:43], off sc1
	v_pk_mul_f32 v[42:43], v[56:57], v[46:47] op_sel_hi:[1,0]
	v_pk_mul_f32 v[44:45], v[54:55], v[46:47] op_sel_hi:[1,0]
	v_pk_fma_f32 v[42:43], v[12:13], v[42:43], v[16:17]
	v_pk_fma_f32 v[44:45], v[10:11], v[44:45], v[14:15]
	v_mad_u64_u32 v[56:57], s[8:9], v73, s3, v[48:49]
	v_cvt_pk_f16_f32 v44, v44, v45
	v_cvt_pk_f16_f32 v45, v42, v43
	global_store_dwordx2 v[64:65], v[44:45], off offset:512 sc1
	v_pk_mul_f32 v[26:27], v[26:27], v[46:47] op_sel_hi:[1,0]
	v_pk_mul_f32 v[28:29], v[28:29], v[46:47] op_sel_hi:[1,0]
	v_pk_fma_f32 v[26:27], v[18:19], v[26:27], v[22:23]
	v_pk_fma_f32 v[28:29], v[20:21], v[28:29], v[24:25]
	v_cvt_pk_f16_f32 v26, v26, v27
	v_cvt_pk_f16_f32 v27, v28, v29
	global_store_dwordx2 v[64:65], v[26:27], off offset:1024 sc1
	s_waitcnt vmcnt(6)
	v_mov_b32_e32 v42, v35
	v_mov_b32_e32 v43, v36
	v_mov_b32_e32 v44, v34
	v_mov_b32_e32 v45, v37
	v_pk_add_f32 v[54:55], v[42:43], v[44:45]
	global_load_dwordx4 v[42:45], v[56:57], off
	v_pk_add_f32 v[54:55], v[54:55], v[54:55] op_sel:[0,1] op_sel_hi:[1,0]
	s_waitcnt vmcnt(5)
	v_mov_b32_e32 v67, v31
	v_mov_b32_e32 v55, v30
	v_pk_add_f32 v[54:55], v[54:55], v[66:67]
	s_waitcnt vmcnt(4)
	v_add_f32_e32 v66, v38, v39
	v_mov_b32_e32 v67, v32
	v_add_f32_e32 v68, v40, v41
	v_mov_b32_e32 v69, v33
	v_pk_add_f32 v[66:67], v[66:67], v[68:69]
	s_nop 0
	v_pk_add_f32 v[54:55], v[54:55], v[66:67]
	s_nop 0
	v_add_f32_e32 v54, v54, v55
	ds_bpermute_b32 v55, v58, v54
	s_waitcnt lgkmcnt(0)
	v_add_f32_e32 v54, v54, v55
	ds_bpermute_b32 v55, v59, v54
	s_waitcnt lgkmcnt(0)
	v_add_f32_e32 v54, v54, v55
	ds_bpermute_b32 v55, v60, v54
	s_waitcnt lgkmcnt(0)
	v_add_f32_e32 v54, v54, v55
	ds_bpermute_b32 v55, v61, v54
	s_waitcnt lgkmcnt(0)
	v_add_f32_e32 v54, v54, v55
	ds_bpermute_b32 v55, v62, v54
	s_waitcnt lgkmcnt(0)
	v_add_f32_e32 v46, v54, v55
	ds_bpermute_b32 v54, v63, v46
	s_waitcnt lgkmcnt(0)
	v_add_f32_e32 v46, v46, v54
	v_fmamk_f32 v34, v46, 0xbaaaaaab, v34
	v_fmamk_f32 v35, v46, 0xbaaaaaab, v35
	v_mul_f32_e32 v26, v34, v34
	v_fmac_f32_e32 v36, 0xbaaaaaab, v46
	v_pk_fma_f32 v[26:27], v[34:35], v[34:35], v[26:27] op_sel_hi:[1,1,0]
	v_fmamk_f32 v37, v46, 0xbaaaaaab, v37
	v_mul_f32_e32 v26, v36, v36
	v_pk_fma_f32 v[28:29], v[36:37], v[36:37], v[26:27] op_sel_hi:[1,1,0]
	v_fmamk_f32 v31, v46, 0xbaaaaaab, v31
	v_fmac_f32_e32 v30, 0xbaaaaaab, v46
	v_mul_f32_e32 v26, v30, v30
	v_mul_f32_e32 v28, v31, v31
	v_fmamk_f32 v38, v46, 0xbaaaaaab, v38
	v_pk_add_f32 v[26:27], v[26:27], v[28:29]
	v_fmamk_f32 v39, v46, 0xbaaaaaab, v39
	v_mul_f32_e32 v28, v38, v38
	v_fmac_f32_e32 v40, 0xbaaaaaab, v46
	v_pk_fma_f32 v[28:29], v[38:39], v[38:39], v[28:29] op_sel_hi:[1,1,0]
	v_fmamk_f32 v41, v46, 0xbaaaaaab, v41
	v_mul_f32_e32 v28, v40, v40
	v_fmamk_f32 v33, v46, 0xbaaaaaab, v33
	v_fmamk_f32 v32, v46, 0xbaaaaaab, v32
	v_pk_fma_f32 v[54:55], v[40:41], v[40:41], v[28:29] op_sel_hi:[1,1,0]
	v_mul_f32_e32 v28, v32, v32
	v_mul_f32_e32 v54, v33, v33
	v_pk_add_f32 v[28:29], v[28:29], v[54:55]
	s_nop 0
	v_pk_add_f32 v[68:69], v[26:27], v[28:29]
	s_waitcnt vmcnt(0)
	v_mov_b32_e32 v26, v43
	v_mov_b32_e32 v27, v44
	v_mov_b32_e32 v28, v42
	v_mov_b32_e32 v29, v45
	v_pk_add_f32 v[26:27], v[26:27], v[28:29]
	s_nop 0
	v_pk_add_f32 v[54:55], v[26:27], v[26:27] op_sel:[0,1] op_sel_hi:[1,0]
	global_load_dwordx4 v[26:29], v[56:57], off offset:2048
	global_load_dwordx4 v[64:67], v[56:57], off offset:1024
	v_mov_b32_e32 v56, v47
	s_waitcnt vmcnt(1)
	v_mov_b32_e32 v55, v26
	v_mov_b32_e32 v57, v27
	v_pk_add_f32 v[54:55], v[54:55], v[56:57]
	s_waitcnt vmcnt(0)
	v_add_f32_e32 v56, v64, v65
	v_mov_b32_e32 v57, v28
	v_add_f32_e32 v70, v66, v67
	v_mov_b32_e32 v71, v29
	v_pk_add_f32 v[56:57], v[56:57], v[70:71]
	s_nop 0
	v_pk_add_f32 v[54:55], v[54:55], v[56:57]
	s_nop 0
	v_add_f32_e32 v46, v54, v55
	ds_bpermute_b32 v54, v58, v46
	s_waitcnt lgkmcnt(0)
	v_add_f32_e32 v46, v46, v54
	ds_bpermute_b32 v54, v59, v46
	s_waitcnt lgkmcnt(0)
	v_add_f32_e32 v46, v46, v54
	ds_bpermute_b32 v54, v60, v46
	s_waitcnt lgkmcnt(0)
	v_add_f32_e32 v46, v46, v54
	ds_bpermute_b32 v54, v61, v46
	s_waitcnt lgkmcnt(0)
	v_add_f32_e32 v46, v46, v54
	ds_bpermute_b32 v54, v62, v46
	s_waitcnt lgkmcnt(0)
	v_add_f32_e32 v46, v46, v54
	ds_bpermute_b32 v54, v63, v46
	s_waitcnt lgkmcnt(0)
	v_add_f32_e32 v74, v46, v54
	v_fmamk_f32 v42, v74, 0xbaaaaaab, v42
	v_fmamk_f32 v43, v74, 0xbaaaaaab, v43
	v_fmac_f32_e32 v44, 0xbaaaaaab, v74
	v_mul_f32_e32 v46, v42, v42
	v_fmamk_f32 v45, v74, 0xbaaaaaab, v45
	v_pk_fma_f32 v[54:55], v[42:43], v[42:43], v[46:47] op_sel_hi:[1,1,0]
	v_mul_f32_e32 v46, v44, v44
	v_pk_fma_f32 v[56:57], v[44:45], v[44:45], v[46:47] op_sel_hi:[1,1,0]
	v_fmamk_f32 v27, v74, 0xbaaaaaab, v27
	v_fmac_f32_e32 v26, 0xbaaaaaab, v74
	v_mul_f32_e32 v54, v26, v26
	v_mul_f32_e32 v56, v27, v27
	v_pk_add_f32 v[70:71], v[54:55], v[56:57]
	v_fmamk_f32 v56, v74, 0xbaaaaaab, v64
	v_fmamk_f32 v57, v74, 0xbaaaaaab, v65
	v_fmamk_f32 v54, v74, 0xbaaaaaab, v28
	v_mul_f32_e32 v28, v56, v56
	v_fmac_f32_e32 v66, 0xbaaaaaab, v74
	v_fmamk_f32 v55, v74, 0xbaaaaaab, v29
	v_pk_fma_f32 v[28:29], v[56:57], v[56:57], v[28:29] op_sel_hi:[1,1,0]
	v_fmamk_f32 v67, v74, 0xbaaaaaab, v67
	v_mul_f32_e32 v28, v66, v66
	v_pk_fma_f32 v[64:65], v[66:67], v[66:67], v[28:29] op_sel_hi:[1,1,0]
	v_mul_f32_e32 v28, v54, v54
	v_mul_f32_e32 v64, v55, v55
	v_pk_add_f32 v[28:29], v[28:29], v[64:65]
	v_mov_b32_e32 v65, v68
	v_pk_add_f32 v[28:29], v[70:71], v[28:29]
	s_nop 0
	v_mov_b32_e32 v64, v28
	v_mov_b32_e32 v68, v29
	v_pk_add_f32 v[28:29], v[64:65], v[68:69]
	ds_bpermute_b32 v65, v58, v29
	ds_bpermute_b32 v64, v58, v28
	v_mov_b32_e32 v68, v47
	s_waitcnt lgkmcnt(0)
	v_pk_add_f32 v[28:29], v[28:29], v[64:65]
	ds_bpermute_b32 v65, v59, v29
	ds_bpermute_b32 v64, v59, v28
	s_waitcnt lgkmcnt(0)
	v_pk_add_f32 v[28:29], v[28:29], v[64:65]
	ds_bpermute_b32 v65, v60, v29
	ds_bpermute_b32 v64, v60, v28
	s_waitcnt lgkmcnt(0)
	v_pk_add_f32 v[28:29], v[28:29], v[64:65]
	ds_bpermute_b32 v65, v61, v29
	ds_bpermute_b32 v64, v61, v28
	s_waitcnt lgkmcnt(0)
	v_pk_add_f32 v[28:29], v[28:29], v[64:65]
	ds_bpermute_b32 v65, v62, v29
	ds_bpermute_b32 v64, v62, v28
	s_waitcnt lgkmcnt(0)
	v_pk_add_f32 v[28:29], v[28:29], v[64:65]
	ds_bpermute_b32 v65, v63, v29
	ds_bpermute_b32 v64, v63, v28
	s_waitcnt lgkmcnt(0)
	v_pk_add_f32 v[28:29], v[28:29], v[64:65]
	s_nop 0
	v_pk_fma_f32 v[28:29], v[28:29], s[4:5], v[52:53] op_sel_hi:[1,0,0]
	s_nop 0
	v_mul_f32_e32 v46, 0x4b800000, v29
	v_cmp_gt_f32_e32 vcc, s5, v29
	s_nop 1
	v_cndmask_b32_e32 v29, v29, v46, vcc
	v_rsq_f32_e32 v29, v29
	s_nop 0
	v_mul_f32_e32 v46, 0x45800000, v29
	v_cndmask_b32_e32 v46, v29, v46, vcc
	v_pk_mul_f32 v[36:37], v[36:37], v[46:47] op_sel_hi:[1,0]
	v_pk_mul_f32 v[34:35], v[34:35], v[46:47] op_sel_hi:[1,0]
	v_pk_fma_f32 v[36:37], v[4:5], v[36:37], v[8:9]
	v_pk_fma_f32 v[34:35], v[2:3], v[34:35], v[6:7]
	v_pk_mul_f32 v[38:39], v[38:39], v[46:47] op_sel_hi:[1,0]
	v_cvt_pk_f16_f32 v34, v34, v35
	v_cvt_pk_f16_f32 v35, v36, v37
	v_mad_u64_u32 v[36:37], s[8:9], v72, s6, v[50:51]
	global_store_dwordx2 v[36:37], v[34:35], off sc1
	v_pk_mul_f32 v[34:35], v[40:41], v[46:47] op_sel_hi:[1,0]
	v_pk_fma_f32 v[38:39], v[10:11], v[38:39], v[14:15]
	v_pk_fma_f32 v[34:35], v[12:13], v[34:35], v[16:17]
	v_or_b32_e32 v72, 6, v1
	v_cvt_pk_f16_f32 v38, v38, v39
	v_cvt_pk_f16_f32 v39, v34, v35
	v_mad_u64_u32 v[40:41], s[8:9], v72, s3, v[48:49]
	global_store_dwordx2 v[36:37], v[38:39], off offset:512 sc1
	v_pk_mul_f32 v[38:39], v[32:33], v[46:47] op_sel_hi:[1,0]
	global_load_dwordx4 v[32:35], v[40:41], off
	v_mul_f32_e32 v29, 0x4b800000, v28
	v_cmp_gt_f32_e32 vcc, s5, v28
	v_pk_mul_f32 v[30:31], v[30:31], v[46:47] op_sel_hi:[1,0]
	v_or_b32_e32 v1, 7, v1
	v_cndmask_b32_e32 v46, v28, v29, vcc
	v_pk_fma_f32 v[28:29], v[20:21], v[38:39], v[24:25]
	v_rsq_f32_e32 v38, v46
	v_pk_fma_f32 v[30:31], v[18:19], v[30:31], v[22:23]
	v_mad_u64_u32 v[48:49], s[8:9], v1, s3, v[48:49]
	v_cvt_pk_f16_f32 v30, v30, v31
	v_cvt_pk_f16_f32 v31, v28, v29
	global_store_dwordx2 v[36:37], v[30:31], off offset:1024 sc1
	global_load_dwordx4 v[28:31], v[40:41], off offset:2048
	v_mul_f32_e32 v36, 0x45800000, v38
	v_cndmask_b32_e32 v46, v38, v36, vcc
	global_load_dwordx4 v[36:39], v[40:41], off offset:1024
	v_pk_mul_f32 v[44:45], v[44:45], v[46:47] op_sel_hi:[1,0]
	v_pk_mul_f32 v[40:41], v[42:43], v[46:47] op_sel_hi:[1,0]
	v_pk_fma_f32 v[42:43], v[4:5], v[44:45], v[8:9]
	v_pk_fma_f32 v[40:41], v[2:3], v[40:41], v[6:7]
	v_mad_u64_u32 v[44:45], s[8:9], v73, s6, v[50:51]
	v_cvt_pk_f16_f32 v40, v40, v41
	v_cvt_pk_f16_f32 v41, v42, v43
	global_store_dwordx2 v[44:45], v[40:41], off sc1
	v_pk_mul_f32 v[64:65], v[66:67], v[46:47] op_sel_hi:[1,0]
	v_pk_mul_f32 v[56:57], v[56:57], v[46:47] op_sel_hi:[1,0]
	v_pk_fma_f32 v[64:65], v[12:13], v[64:65], v[16:17]
	v_pk_fma_f32 v[56:57], v[10:11], v[56:57], v[14:15]
	v_pk_mul_f32 v[26:27], v[26:27], v[46:47] op_sel_hi:[1,0]
	v_cvt_pk_f16_f32 v56, v56, v57
	v_cvt_pk_f16_f32 v57, v64, v65
	v_pk_mul_f32 v[54:55], v[54:55], v[46:47] op_sel_hi:[1,0]
	global_store_dwordx2 v[44:45], v[56:57], off offset:512 sc1
	v_pk_fma_f32 v[54:55], v[20:21], v[54:55], v[24:25]
	v_pk_fma_f32 v[26:27], v[18:19], v[26:27], v[22:23]
	s_waitcnt vmcnt(5)
	v_mov_b32_e32 v40, v33
	v_mov_b32_e32 v41, v34
	v_mov_b32_e32 v42, v32
	v_mov_b32_e32 v43, v35
	v_pk_add_f32 v[66:67], v[40:41], v[42:43]
	global_load_dwordx4 v[40:43], v[48:49], off
	v_pk_add_f32 v[66:67], v[66:67], v[66:67] op_sel:[0,1] op_sel_hi:[1,0]
	v_cvt_pk_f16_f32 v26, v26, v27
	v_cvt_pk_f16_f32 v27, v54, v55
	s_waitcnt vmcnt(4)
	v_mov_b32_e32 v67, v28
	v_mov_b32_e32 v69, v29
	v_pk_add_f32 v[66:67], v[66:67], v[68:69]
	s_waitcnt vmcnt(3)
	v_add_f32_e32 v68, v36, v37
	v_mov_b32_e32 v69, v30
	v_add_f32_e32 v70, v38, v39
	v_mov_b32_e32 v71, v31
	v_pk_add_f32 v[68:69], v[68:69], v[70:71]
	s_nop 0
	v_pk_add_f32 v[66:67], v[66:67], v[68:69]
	s_nop 0
	v_add_f32_e32 v66, v66, v67
	ds_bpermute_b32 v67, v58, v66
	s_waitcnt lgkmcnt(0)
	v_add_f32_e32 v66, v66, v67
	ds_bpermute_b32 v67, v59, v66
	s_waitcnt lgkmcnt(0)
	v_add_f32_e32 v66, v66, v67
	ds_bpermute_b32 v67, v60, v66
	s_waitcnt lgkmcnt(0)
	v_add_f32_e32 v66, v66, v67
	ds_bpermute_b32 v67, v61, v66
	s_waitcnt lgkmcnt(0)
	v_add_f32_e32 v66, v66, v67
	ds_bpermute_b32 v67, v62, v66
	s_waitcnt lgkmcnt(0)
	v_add_f32_e32 v46, v66, v67
	ds_bpermute_b32 v56, v63, v46
	s_waitcnt lgkmcnt(0)
	v_add_f32_e32 v46, v46, v56
	v_fmamk_f32 v64, v46, 0xbaaaaaab, v32
	v_fmamk_f32 v65, v46, 0xbaaaaaab, v33
	v_mul_f32_e32 v32, v64, v64
	v_fmac_f32_e32 v34, 0xbaaaaaab, v46
	v_pk_fma_f32 v[32:33], v[64:65], v[64:65], v[32:33] op_sel_hi:[1,1,0]
	v_fmamk_f32 v36, v46, 0xbaaaaaab, v36
	v_fmamk_f32 v35, v46, 0xbaaaaaab, v35
	v_mul_f32_e32 v32, v34, v34
	v_fmamk_f32 v37, v46, 0xbaaaaaab, v37
	v_fmamk_f32 v66, v46, 0xbaaaaaab, v30
	v_mul_f32_e32 v30, v36, v36
	v_pk_fma_f32 v[54:55], v[34:35], v[34:35], v[32:33] op_sel_hi:[1,1,0]
	v_fmamk_f32 v29, v46, 0xbaaaaaab, v29
	v_fmac_f32_e32 v28, 0xbaaaaaab, v46
	v_fmac_f32_e32 v38, 0xbaaaaaab, v46
	v_fmamk_f32 v67, v46, 0xbaaaaaab, v31
	v_pk_fma_f32 v[30:31], v[36:37], v[36:37], v[30:31] op_sel_hi:[1,1,0]
	v_mul_f32_e32 v32, v28, v28
	v_mul_f32_e32 v54, v29, v29
	v_fmamk_f32 v39, v46, 0xbaaaaaab, v39
	v_mul_f32_e32 v30, v38, v38
	v_pk_add_f32 v[32:33], v[32:33], v[54:55]
	v_pk_fma_f32 v[54:55], v[38:39], v[38:39], v[30:31] op_sel_hi:[1,1,0]
	v_mul_f32_e32 v30, v66, v66
	v_mul_f32_e32 v54, v67, v67
	v_pk_add_f32 v[30:31], v[30:31], v[54:55]
	v_mov_b32_e32 v46, v47
	v_pk_add_f32 v[68:69], v[32:33], v[30:31]
	s_waitcnt vmcnt(0)
	v_mov_b32_e32 v30, v41
	v_mov_b32_e32 v31, v42
	v_mov_b32_e32 v32, v40
	v_mov_b32_e32 v33, v43
	v_pk_add_f32 v[30:31], v[30:31], v[32:33]
	s_nop 0
	v_pk_add_f32 v[70:71], v[30:31], v[30:31] op_sel:[0,1] op_sel_hi:[1,0]
	global_load_dwordx4 v[30:33], v[48:49], off offset:2048
	global_load_dwordx4 v[54:57], v[48:49], off offset:1024
	s_waitcnt vmcnt(1)
	v_mov_b32_e32 v71, v30
	v_mov_b32_e32 v47, v31
	v_pk_add_f32 v[46:47], v[70:71], v[46:47]
	s_waitcnt vmcnt(0)
	v_add_f32_e32 v48, v54, v55
	v_mov_b32_e32 v49, v32
	v_add_f32_e32 v70, v56, v57
	v_mov_b32_e32 v71, v33
	v_pk_add_f32 v[48:49], v[48:49], v[70:71]
	global_store_dwordx2 v[44:45], v[26:27], off offset:1024 sc1
	v_pk_add_f32 v[46:47], v[46:47], v[48:49]
	s_nop 0
	v_add_f32_e32 v46, v46, v47
	ds_bpermute_b32 v47, v58, v46
	s_waitcnt lgkmcnt(0)
	v_add_f32_e32 v46, v46, v47
	ds_bpermute_b32 v47, v59, v46
	s_waitcnt lgkmcnt(0)
	v_add_f32_e32 v46, v46, v47
	ds_bpermute_b32 v47, v60, v46
	s_waitcnt lgkmcnt(0)
	v_add_f32_e32 v46, v46, v47
	ds_bpermute_b32 v47, v61, v46
	s_waitcnt lgkmcnt(0)
	v_add_f32_e32 v46, v46, v47
	ds_bpermute_b32 v47, v62, v46
	s_waitcnt lgkmcnt(0)
	v_add_f32_e32 v46, v46, v47
	ds_bpermute_b32 v47, v63, v46
	s_waitcnt lgkmcnt(0)
	v_add_f32_e32 v70, v46, v47
	v_fmamk_f32 v40, v70, 0xbaaaaaab, v40
	v_fmamk_f32 v41, v70, 0xbaaaaaab, v41
	v_mul_f32_e32 v46, v40, v40
	v_fmac_f32_e32 v42, 0xbaaaaaab, v70
	v_pk_fma_f32 v[46:47], v[40:41], v[40:41], v[46:47] op_sel_hi:[1,1,0]
	v_fmamk_f32 v43, v70, 0xbaaaaaab, v43
	v_mul_f32_e32 v46, v42, v42
	v_pk_fma_f32 v[48:49], v[42:43], v[42:43], v[46:47] op_sel_hi:[1,1,0]
	v_fmamk_f32 v31, v70, 0xbaaaaaab, v31
	v_fmac_f32_e32 v30, 0xbaaaaaab, v70
	v_mul_f32_e32 v46, v30, v30
	v_mul_f32_e32 v48, v31, v31
	v_pk_add_f32 v[46:47], v[46:47], v[48:49]
	v_fmamk_f32 v48, v70, 0xbaaaaaab, v54
	v_fmamk_f32 v49, v70, 0xbaaaaaab, v55
	v_mul_f32_e32 v54, v48, v48
	v_fmac_f32_e32 v56, 0xbaaaaaab, v70
	v_pk_fma_f32 v[54:55], v[48:49], v[48:49], v[54:55] op_sel_hi:[1,1,0]
	v_fmamk_f32 v57, v70, 0xbaaaaaab, v57
	v_mul_f32_e32 v54, v56, v56
	v_fmamk_f32 v33, v70, 0xbaaaaaab, v33
	v_fmamk_f32 v32, v70, 0xbaaaaaab, v32
	v_pk_fma_f32 v[70:71], v[56:57], v[56:57], v[54:55] op_sel_hi:[1,1,0]
	v_mul_f32_e32 v54, v32, v32
	v_mul_f32_e32 v70, v33, v33
	v_pk_add_f32 v[54:55], v[54:55], v[70:71]
	s_nop 0
	v_pk_add_f32 v[46:47], v[46:47], v[54:55]
	v_mov_b32_e32 v55, v68
	v_mov_b32_e32 v54, v46
	v_mov_b32_e32 v68, v47
	v_pk_add_f32 v[46:47], v[54:55], v[68:69]
	ds_bpermute_b32 v55, v58, v47
	ds_bpermute_b32 v54, v58, v46
	s_waitcnt lgkmcnt(0)
	v_pk_add_f32 v[46:47], v[46:47], v[54:55]
	ds_bpermute_b32 v55, v59, v47
	ds_bpermute_b32 v54, v59, v46
	s_waitcnt lgkmcnt(0)
	v_pk_add_f32 v[46:47], v[46:47], v[54:55]
	ds_bpermute_b32 v55, v60, v47
	ds_bpermute_b32 v54, v60, v46
	s_waitcnt lgkmcnt(0)
	v_pk_add_f32 v[46:47], v[46:47], v[54:55]
	ds_bpermute_b32 v55, v61, v47
	ds_bpermute_b32 v54, v61, v46
	s_waitcnt lgkmcnt(0)
	v_pk_add_f32 v[46:47], v[46:47], v[54:55]
	ds_bpermute_b32 v55, v62, v47
	ds_bpermute_b32 v54, v62, v46
	s_waitcnt lgkmcnt(0)
	v_pk_add_f32 v[46:47], v[46:47], v[54:55]
	ds_bpermute_b32 v55, v63, v47
	ds_bpermute_b32 v54, v63, v46
	s_waitcnt lgkmcnt(0)
	v_pk_add_f32 v[46:47], v[46:47], v[54:55]
	s_nop 0
	v_pk_fma_f32 v[46:47], v[46:47], s[4:5], v[52:53] op_sel_hi:[1,0,0]
	s_nop 0
	v_mul_f32_e32 v52, 0x4b800000, v47
	v_cmp_gt_f32_e32 vcc, s5, v47
	s_nop 1
	v_cndmask_b32_e32 v47, v47, v52, vcc
	v_rsq_f32_e32 v47, v47
	s_nop 0
	v_mul_f32_e32 v26, 0x45800000, v47
	v_cndmask_b32_e32 v26, v47, v26, vcc
	v_pk_mul_f32 v[34:35], v[34:35], v[26:27] op_sel_hi:[1,0]
	v_pk_mul_f32 v[44:45], v[64:65], v[26:27] op_sel_hi:[1,0]
	v_pk_mul_f32 v[38:39], v[38:39], v[26:27] op_sel_hi:[1,0]
	v_pk_mul_f32 v[36:37], v[36:37], v[26:27] op_sel_hi:[1,0]
	v_pk_fma_f32 v[34:35], v[4:5], v[34:35], v[8:9]
	v_pk_fma_f32 v[44:45], v[2:3], v[44:45], v[6:7]
	v_pk_fma_f32 v[38:39], v[12:13], v[38:39], v[16:17]
	v_pk_fma_f32 v[36:37], v[10:11], v[36:37], v[14:15]
	v_cvt_pk_f16_f32 v44, v44, v45
	v_cvt_pk_f16_f32 v45, v34, v35
	v_mad_u64_u32 v[34:35], s[8:9], v72, s6, v[50:51]
	v_cvt_pk_f16_f32 v36, v36, v37
	v_cvt_pk_f16_f32 v37, v38, v39
	global_store_dwordx2 v[34:35], v[36:37], off offset:512 sc1
	v_mul_f32_e32 v36, 0x4b800000, v46
	v_cmp_gt_f32_e32 vcc, s5, v46
	v_pk_mul_f32 v[28:29], v[28:29], v[26:27] op_sel_hi:[1,0]
	v_pk_mul_f32 v[26:27], v[66:67], v[26:27] op_sel_hi:[1,0]
	v_cndmask_b32_e32 v36, v46, v36, vcc
	v_rsq_f32_e32 v36, v36
	v_pk_fma_f32 v[26:27], v[20:21], v[26:27], v[24:25]
	v_pk_fma_f32 v[28:29], v[18:19], v[28:29], v[22:23]
	global_store_dwordx2 v[34:35], v[44:45], off sc1
	v_cvt_pk_f16_f32 v28, v28, v29
	v_cvt_pk_f16_f32 v29, v26, v27
	v_mul_f32_e32 v26, 0x45800000, v36
	v_cndmask_b32_e32 v26, v36, v26, vcc
	global_store_dwordx2 v[34:35], v[28:29], off offset:1024 sc1
	v_pk_mul_f32 v[34:35], v[40:41], v[26:27] op_sel_hi:[1,0]
	v_pk_mul_f32 v[36:37], v[42:43], v[26:27] op_sel_hi:[1,0]
	v_pk_fma_f32 v[2:3], v[2:3], v[34:35], v[6:7]
	v_pk_fma_f32 v[4:5], v[4:5], v[36:37], v[8:9]
	v_mad_u64_u32 v[28:29], s[4:5], v1, s6, v[50:51]
	v_cvt_pk_f16_f32 v2, v2, v3
	v_cvt_pk_f16_f32 v3, v4, v5
	global_store_dwordx2 v[28:29], v[2:3], off sc1
	v_pk_mul_f32 v[2:3], v[48:49], v[26:27] op_sel_hi:[1,0]
	v_pk_mul_f32 v[4:5], v[56:57], v[26:27] op_sel_hi:[1,0]
	v_pk_fma_f32 v[2:3], v[10:11], v[2:3], v[14:15]
	v_pk_fma_f32 v[4:5], v[12:13], v[4:5], v[16:17]
	v_cvt_pk_f16_f32 v2, v2, v3
	v_cvt_pk_f16_f32 v3, v4, v5
	global_store_dwordx2 v[28:29], v[2:3], off offset:512 sc1
	v_pk_mul_f32 v[2:3], v[30:31], v[26:27] op_sel_hi:[1,0]
	v_pk_mul_f32 v[4:5], v[32:33], v[26:27] op_sel_hi:[1,0]
	v_pk_fma_f32 v[2:3], v[18:19], v[2:3], v[22:23]
	v_pk_fma_f32 v[4:5], v[20:21], v[4:5], v[24:25]
	v_cvt_pk_f16_f32 v2, v2, v3
	v_cvt_pk_f16_f32 v3, v4, v5
	s_mov_b64 s[4:5], 0
	global_store_dwordx2 v[28:29], v[2:3], off offset:1024 sc1
